# placement: 64-byte alignment of the four bf16/fp8 K-loop heads entered by back-branch (P2, P3, P7, P8)
# speedup vs baseline: 1.0017x; 1.0002x over previous
.LBB0_284:
	s_ashr_i32 s43, s42, 31
	s_lshl_b64 s[48:49], s[42:43], 19
	s_add_u32 s48, s85, s48
	s_addc_u32 s49, s86, s49
	s_and_b64 s[52:53], s[46:47], exec
	s_cselect_b32 s43, s49, s59
	s_cselect_b32 s57, s48, s58
	s_ashr_i32 s45, s44, 31
	s_lshl_b64 s[52:53], s[44:45], 19
	s_add_u32 s52, s87, s52
	s_addc_u32 s53, s89, s53
	s_and_b64 s[66:67], s[46:47], exec
	s_cselect_b32 s45, s53, s63
	s_cselect_b32 s68, s52, s62
	s_add_u32 s58, s58, 0x40080
	s_addc_u32 s59, s59, 0
	s_add_u32 s69, s62, 0x100
	v_mov_b32_e32 v34, 0
	s_addc_u32 s70, s63, 0
	s_mov_b32 s71, -2
	v_mov_b32_e32 v35, v34
	v_mov_b32_e32 v36, v34
	v_mov_b32_e32 v37, v34
	v_mov_b32_e32 v38, v34
	v_mov_b32_e32 v39, v34
	v_mov_b32_e32 v40, v34
	v_mov_b32_e32 v41, v34
	v_mov_b32_e32 v42, v34
	v_mov_b32_e32 v43, v34
	v_mov_b32_e32 v44, v34
	v_mov_b32_e32 v45, v34
	v_mov_b32_e32 v46, v34
	v_mov_b32_e32 v47, v34
	v_mov_b32_e32 v48, v34
	v_mov_b32_e32 v49, v34
	v_mov_b32_e32 v62, v34
	v_mov_b32_e32 v63, v34
	v_mov_b32_e32 v64, v34
	v_mov_b32_e32 v65, v34
	v_mov_b32_e32 v70, v34
	v_mov_b32_e32 v71, v34
	v_mov_b32_e32 v72, v34
	v_mov_b32_e32 v73, v34
	v_mov_b32_e32 v74, v34
	v_mov_b32_e32 v75, v34
	v_mov_b32_e32 v76, v34
	v_mov_b32_e32 v77, v34
	v_mov_b32_e32 v78, v34
	v_mov_b32_e32 v79, v34
	v_mov_b32_e32 v80, v34
	v_mov_b32_e32 v81, v34
	v_mov_b32_e32 v50, v34
	v_mov_b32_e32 v51, v34
	v_mov_b32_e32 v52, v34
	v_mov_b32_e32 v53, v34
	v_mov_b32_e32 v54, v34
	v_mov_b32_e32 v55, v34
	v_mov_b32_e32 v56, v34
	v_mov_b32_e32 v57, v34
	v_mov_b32_e32 v58, v34
	v_mov_b32_e32 v59, v34
	v_mov_b32_e32 v60, v34
	v_mov_b32_e32 v61, v34
	v_mov_b32_e32 v66, v34
	v_mov_b32_e32 v67, v34
	v_mov_b32_e32 v68, v34
	v_mov_b32_e32 v69, v34
	v_mov_b32_e32 v82, v34
	v_mov_b32_e32 v83, v34
	v_mov_b32_e32 v84, v34
	v_mov_b32_e32 v85, v34
	v_mov_b32_e32 v86, v34
	v_mov_b32_e32 v87, v34
	v_mov_b32_e32 v88, v34
	v_mov_b32_e32 v89, v34
	v_mov_b32_e32 v90, v34
	v_mov_b32_e32 v91, v34
	v_mov_b32_e32 v92, v34
	v_mov_b32_e32 v93, v34
	v_mov_b32_e32 v94, v34
	v_mov_b32_e32 v95, v34
	v_mov_b32_e32 v96, v34
	v_mov_b32_e32 v97, v34
	v_mov_b32_e32 v98, v34
	v_mov_b32_e32 v99, v34
	v_mov_b32_e32 v100, v34
	v_mov_b32_e32 v101, v34
	v_mov_b32_e32 v102, v34
	v_mov_b32_e32 v103, v34
	v_mov_b32_e32 v104, v34
	v_mov_b32_e32 v105, v34
	v_mov_b32_e32 v106, v34
	v_mov_b32_e32 v107, v34
	v_mov_b32_e32 v108, v34
	v_mov_b32_e32 v109, v34
	v_mov_b32_e32 v110, v34
	v_mov_b32_e32 v111, v34
	v_mov_b32_e32 v112, v34
	v_mov_b32_e32 v113, v34
	v_mov_b32_e32 v126, v34
	v_mov_b32_e32 v127, v34
	v_mov_b32_e32 v128, v34
	v_mov_b32_e32 v129, v34
	v_mov_b32_e32 v134, v34
	v_mov_b32_e32 v135, v34
	v_mov_b32_e32 v136, v34
	v_mov_b32_e32 v137, v34
	v_mov_b32_e32 v138, v34
	v_mov_b32_e32 v139, v34
	v_mov_b32_e32 v140, v34
	v_mov_b32_e32 v141, v34
	v_mov_b32_e32 v142, v34
	v_mov_b32_e32 v143, v34
	v_mov_b32_e32 v144, v34
	v_mov_b32_e32 v145, v34
	v_mov_b32_e32 v114, v34
	v_mov_b32_e32 v115, v34
	v_mov_b32_e32 v116, v34
	v_mov_b32_e32 v117, v34
	v_mov_b32_e32 v118, v34
	v_mov_b32_e32 v119, v34
	v_mov_b32_e32 v120, v34
	v_mov_b32_e32 v121, v34
	v_mov_b32_e32 v122, v34
	v_mov_b32_e32 v123, v34
	v_mov_b32_e32 v124, v34
	v_mov_b32_e32 v125, v34
	v_mov_b32_e32 v130, v34
	v_mov_b32_e32 v131, v34
	v_mov_b32_e32 v132, v34
	v_mov_b32_e32 v133, v34
	v_mov_b32_e32 v146, v34
	v_mov_b32_e32 v147, v34
	v_mov_b32_e32 v148, v34
	v_mov_b32_e32 v149, v34
	v_mov_b32_e32 v150, v34
	v_mov_b32_e32 v151, v34
	v_mov_b32_e32 v152, v34
	v_mov_b32_e32 v153, v34
	v_mov_b32_e32 v154, v34
	v_mov_b32_e32 v155, v34
	v_mov_b32_e32 v156, v34
	v_mov_b32_e32 v157, v34
	v_mov_b32_e32 v158, v34
	v_mov_b32_e32 v159, v34
	v_mov_b32_e32 v160, v34
	v_mov_b32_e32 v161, v34
	.p2align 6

.LBB0_335:
	s_ashr_i32 s17, s16, 31
	s_lshl_b64 s[40:41], s[16:17], 20
	s_add_u32 s40, s31, s40
	s_addc_u32 s41, s34, s41
	s_and_b64 s[44:45], s[42:43], exec
	s_cselect_b32 s17, s41, s49
	s_cselect_b32 s56, s40, s48
	s_ashr_i32 s39, s38, 31
	s_lshl_b64 s[44:45], s[38:39], 20
	s_add_u32 s44, s35, s44
	s_addc_u32 s45, s62, s45
	s_and_b64 s[54:55], s[42:43], exec
	s_cselect_b32 s39, s45, s53
	s_cselect_b32 s57, s44, s52
	s_add_u32 s48, s48, 0x80080
	s_addc_u32 s49, s49, 0
	s_add_u32 s58, s52, 0x100
	v_mov_b32_e32 v2, 0
	s_addc_u32 s59, s53, 0
	s_mov_b32 s87, -2
	v_mov_b32_e32 v3, v2
	v_mov_b32_e32 v4, v2
	v_mov_b32_e32 v5, v2
	v_mov_b32_e32 v6, v2
	v_mov_b32_e32 v7, v2
	v_mov_b32_e32 v8, v2
	v_mov_b32_e32 v9, v2
	v_mov_b32_e32 v14, v2
	v_mov_b32_e32 v15, v2
	v_mov_b32_e32 v16, v2
	v_mov_b32_e32 v17, v2
	v_mov_b32_e32 v22, v2
	v_mov_b32_e32 v23, v2
	v_mov_b32_e32 v24, v2
	v_mov_b32_e32 v25, v2
	v_mov_b32_e32 v30, v2
	v_mov_b32_e32 v31, v2
	v_mov_b32_e32 v32, v2
	v_mov_b32_e32 v33, v2
	v_mov_b32_e32 v38, v2
	v_mov_b32_e32 v39, v2
	v_mov_b32_e32 v40, v2
	v_mov_b32_e32 v41, v2
	v_mov_b32_e32 v46, v2
	v_mov_b32_e32 v47, v2
	v_mov_b32_e32 v48, v2
	v_mov_b32_e32 v49, v2
	v_mov_b32_e32 v54, v2
	v_mov_b32_e32 v55, v2
	v_mov_b32_e32 v56, v2
	v_mov_b32_e32 v57, v2
	v_mov_b32_e32 v10, v2
	v_mov_b32_e32 v11, v2
	v_mov_b32_e32 v12, v2
	v_mov_b32_e32 v13, v2
	v_mov_b32_e32 v18, v2
	v_mov_b32_e32 v19, v2
	v_mov_b32_e32 v20, v2
	v_mov_b32_e32 v21, v2
	v_mov_b32_e32 v26, v2
	v_mov_b32_e32 v27, v2
	v_mov_b32_e32 v28, v2
	v_mov_b32_e32 v29, v2
	v_mov_b32_e32 v34, v2
	v_mov_b32_e32 v35, v2
	v_mov_b32_e32 v36, v2
	v_mov_b32_e32 v37, v2
	v_mov_b32_e32 v42, v2
	v_mov_b32_e32 v43, v2
	v_mov_b32_e32 v44, v2
	v_mov_b32_e32 v45, v2
	v_mov_b32_e32 v50, v2
	v_mov_b32_e32 v51, v2
	v_mov_b32_e32 v52, v2
	v_mov_b32_e32 v53, v2
	v_mov_b32_e32 v58, v2
	v_mov_b32_e32 v59, v2
	v_mov_b32_e32 v60, v2
	v_mov_b32_e32 v61, v2
	v_mov_b32_e32 v62, v2
	v_mov_b32_e32 v63, v2
	v_mov_b32_e32 v64, v2
	v_mov_b32_e32 v65, v2
	v_mov_b32_e32 v66, v2
	v_mov_b32_e32 v67, v2
	v_mov_b32_e32 v68, v2
	v_mov_b32_e32 v69, v2
	v_mov_b32_e32 v70, v2
	v_mov_b32_e32 v71, v2
	v_mov_b32_e32 v72, v2
	v_mov_b32_e32 v73, v2
	v_mov_b32_e32 v78, v2
	v_mov_b32_e32 v79, v2
	v_mov_b32_e32 v80, v2
	v_mov_b32_e32 v81, v2
	v_mov_b32_e32 v86, v2
	v_mov_b32_e32 v87, v2
	v_mov_b32_e32 v88, v2
	v_mov_b32_e32 v89, v2
	v_mov_b32_e32 v94, v2
	v_mov_b32_e32 v95, v2
	v_mov_b32_e32 v96, v2
	v_mov_b32_e32 v97, v2
	v_mov_b32_e32 v102, v2
	v_mov_b32_e32 v103, v2
	v_mov_b32_e32 v104, v2
	v_mov_b32_e32 v105, v2
	v_mov_b32_e32 v110, v2
	v_mov_b32_e32 v111, v2
	v_mov_b32_e32 v112, v2
	v_mov_b32_e32 v113, v2
	v_mov_b32_e32 v118, v2
	v_mov_b32_e32 v119, v2
	v_mov_b32_e32 v120, v2
	v_mov_b32_e32 v121, v2
	v_mov_b32_e32 v74, v2
	v_mov_b32_e32 v75, v2
	v_mov_b32_e32 v76, v2
	v_mov_b32_e32 v77, v2
	v_mov_b32_e32 v82, v2
	v_mov_b32_e32 v83, v2
	v_mov_b32_e32 v84, v2
	v_mov_b32_e32 v85, v2
	v_mov_b32_e32 v90, v2
	v_mov_b32_e32 v91, v2
	v_mov_b32_e32 v92, v2
	v_mov_b32_e32 v93, v2
	v_mov_b32_e32 v98, v2
	v_mov_b32_e32 v99, v2
	v_mov_b32_e32 v100, v2
	v_mov_b32_e32 v101, v2
	v_mov_b32_e32 v106, v2
	v_mov_b32_e32 v107, v2
	v_mov_b32_e32 v108, v2
	v_mov_b32_e32 v109, v2
	v_mov_b32_e32 v114, v2
	v_mov_b32_e32 v115, v2
	v_mov_b32_e32 v116, v2
	v_mov_b32_e32 v117, v2
	v_mov_b32_e32 v122, v2
	v_mov_b32_e32 v123, v2
	v_mov_b32_e32 v124, v2
	v_mov_b32_e32 v125, v2
	v_mov_b32_e32 v126, v2
	v_mov_b32_e32 v127, v2
	v_mov_b32_e32 v128, v2
	v_mov_b32_e32 v129, v2
	.p2align 6

.LBB0_845:
	s_ashr_i32 s45, s44, 31
	s_lshl_b64 s[34:35], s[44:45], 20
	s_add_u32 s48, s3, s34
	s_addc_u32 s49, s66, s35
	s_and_b64 s[34:35], s[6:7], exec
	s_cselect_b32 s34, s49, s55
	s_cselect_b32 s35, s48, s54
	s_ashr_i32 s47, s46, 31
	s_lshl_b64 s[52:53], s[46:47], 20
	s_add_u32 s52, s67, s52
	s_addc_u32 s53, s68, s53
	s_and_b64 s[62:63], s[6:7], exec
	s_cselect_b32 s45, s53, s59
	s_cselect_b32 s47, s52, s58
	s_add_u32 s54, s54, 0x80080
	s_addc_u32 s55, s55, 0
	s_add_u32 s57, s58, 0x100
	s_addc_u32 s86, s59, 0
	s_mov_b32 s87, -2
	.p2align 6

.LBB0_926:
	s_ashr_i32 s47, s46, 31
	s_lshl_b64 s[48:49], s[46:47], 20
	s_add_u32 s48, s3, s48
	s_addc_u32 s49, s30, s49
	s_and_b64 s[52:53], s[6:7], exec
	s_cselect_b32 s47, s49, s57
	s_cselect_b32 s82, s48, s56
	s_ashr_i32 s45, s44, 31
	s_lshl_b64 s[52:53], s[44:45], 20
	s_add_u32 s52, s31, s52
	s_addc_u32 s53, s34, s53
	s_and_b64 s[62:63], s[6:7], exec
	s_cselect_b32 s45, s53, s59
	s_cselect_b32 s83, s52, s58
	s_add_u32 s56, s56, 0x80080
	s_addc_u32 s57, s57, 0
	s_add_u32 s84, s58, 0x100
	v_mov_b32_e32 v2, 0
	s_addc_u32 s85, s59, 0
	s_mov_b32 s86, -2
	v_mov_b32_e32 v3, v2
	v_mov_b32_e32 v4, v2
	v_mov_b32_e32 v5, v2
	v_mov_b32_e32 v6, v2
	v_mov_b32_e32 v7, v2
	v_mov_b32_e32 v8, v2
	v_mov_b32_e32 v9, v2
	v_mov_b32_e32 v14, v2
	v_mov_b32_e32 v15, v2
	v_mov_b32_e32 v16, v2
	v_mov_b32_e32 v17, v2
	v_mov_b32_e32 v22, v2
	v_mov_b32_e32 v23, v2
	v_mov_b32_e32 v24, v2
	v_mov_b32_e32 v25, v2
	v_mov_b32_e32 v30, v2
	v_mov_b32_e32 v31, v2
	v_mov_b32_e32 v32, v2
	v_mov_b32_e32 v33, v2
	v_mov_b32_e32 v38, v2
	v_mov_b32_e32 v39, v2
	v_mov_b32_e32 v40, v2
	v_mov_b32_e32 v41, v2
	v_mov_b32_e32 v46, v2
	v_mov_b32_e32 v47, v2
	v_mov_b32_e32 v48, v2
	v_mov_b32_e32 v49, v2
	v_mov_b32_e32 v54, v2
	v_mov_b32_e32 v55, v2
	v_mov_b32_e32 v56, v2
	v_mov_b32_e32 v57, v2
	v_mov_b32_e32 v10, v2
	v_mov_b32_e32 v11, v2
	v_mov_b32_e32 v12, v2
	v_mov_b32_e32 v13, v2
	v_mov_b32_e32 v18, v2
	v_mov_b32_e32 v19, v2
	v_mov_b32_e32 v20, v2
	v_mov_b32_e32 v21, v2
	v_mov_b32_e32 v26, v2
	v_mov_b32_e32 v27, v2
	v_mov_b32_e32 v28, v2
	v_mov_b32_e32 v29, v2
	v_mov_b32_e32 v34, v2
	v_mov_b32_e32 v35, v2
	v_mov_b32_e32 v36, v2
	v_mov_b32_e32 v37, v2
	v_mov_b32_e32 v42, v2
	v_mov_b32_e32 v43, v2
	v_mov_b32_e32 v44, v2
	v_mov_b32_e32 v45, v2
	v_mov_b32_e32 v50, v2
	v_mov_b32_e32 v51, v2
	v_mov_b32_e32 v52, v2
	v_mov_b32_e32 v53, v2
	v_mov_b32_e32 v58, v2
	v_mov_b32_e32 v59, v2
	v_mov_b32_e32 v60, v2
	v_mov_b32_e32 v61, v2
	v_mov_b32_e32 v62, v2
	v_mov_b32_e32 v63, v2
	v_mov_b32_e32 v64, v2
	v_mov_b32_e32 v65, v2
	v_mov_b32_e32 v66, v2
	v_mov_b32_e32 v67, v2
	v_mov_b32_e32 v68, v2
	v_mov_b32_e32 v69, v2
	v_mov_b32_e32 v70, v2
	v_mov_b32_e32 v71, v2
	v_mov_b32_e32 v72, v2
	v_mov_b32_e32 v73, v2
	v_mov_b32_e32 v78, v2
	v_mov_b32_e32 v79, v2
	v_mov_b32_e32 v80, v2
	v_mov_b32_e32 v81, v2
	v_mov_b32_e32 v86, v2
	v_mov_b32_e32 v87, v2
	v_mov_b32_e32 v88, v2
	v_mov_b32_e32 v89, v2
	v_mov_b32_e32 v82, v2
	v_mov_b32_e32 v83, v2
	v_mov_b32_e32 v84, v2
	v_mov_b32_e32 v85, v2
	v_mov_b32_e32 v98, v2
	v_mov_b32_e32 v99, v2
	v_mov_b32_e32 v100, v2
	v_mov_b32_e32 v101, v2
	v_mov_b32_e32 v90, v2
	v_mov_b32_e32 v91, v2
	v_mov_b32_e32 v92, v2
	v_mov_b32_e32 v93, v2
	v_mov_b32_e32 v106, v2
	v_mov_b32_e32 v107, v2
	v_mov_b32_e32 v108, v2
	v_mov_b32_e32 v109, v2
	v_mov_b32_e32 v74, v2
	v_mov_b32_e32 v75, v2
	v_mov_b32_e32 v76, v2
	v_mov_b32_e32 v77, v2
	v_mov_b32_e32 v94, v2
	v_mov_b32_e32 v95, v2
	v_mov_b32_e32 v96, v2
	v_mov_b32_e32 v97, v2
	v_mov_b32_e32 v110, v2
	v_mov_b32_e32 v111, v2
	v_mov_b32_e32 v112, v2
	v_mov_b32_e32 v113, v2
	v_mov_b32_e32 v102, v2
	v_mov_b32_e32 v103, v2
	v_mov_b32_e32 v104, v2
	v_mov_b32_e32 v105, v2
	v_mov_b32_e32 v118, v2
	v_mov_b32_e32 v119, v2
	v_mov_b32_e32 v120, v2
	v_mov_b32_e32 v121, v2
	v_mov_b32_e32 v114, v2
	v_mov_b32_e32 v115, v2
	v_mov_b32_e32 v116, v2
	v_mov_b32_e32 v117, v2
	v_mov_b32_e32 v126, v2
	v_mov_b32_e32 v127, v2
	v_mov_b32_e32 v128, v2
	v_mov_b32_e32 v129, v2
	v_mov_b32_e32 v122, v2
	v_mov_b32_e32 v123, v2
	v_mov_b32_e32 v124, v2
	v_mov_b32_e32 v125, v2
	.p2align 6
